# E40: E25 + post-barrier trim in the rotated far loops: the m0 write for the first LDS-DMA and the DMA-flag compare are issued before the tile-end barrier
# speedup vs baseline: 1.0107x; 1.0107x over previous
.Lx687_pd:
	s_mov_b32 m0, s100
	s_cmp_eq_u32 s32, 0
	s_waitcnt vmcnt(0)
	s_barrier
	ds_read_b128 v[70:73], v0
	ds_read_b128 v[74:77], v0 offset:4096
	ds_read_b128 v[78:81], v197
	ds_read_b128 v[82:85], v197 offset:4096
	ds_read_b128 v[86:89], v0 offset:8192
	ds_read_b128 v[94:97], v0 offset:12288
	s_cbranch_scc1 .Lr687_skip
	global_load_lds_dwordx4 v[240:241], off
	s_add_i32 m0, s100, 0x400
	s_nop 0
	global_load_lds_dwordx4 v[242:243], off
	s_mov_b32 m0, s101
	s_nop 0
	global_load_lds_dwordx4 v[244:245], off
	s_add_i32 m0, s101, 0x400
	s_nop 0
	global_load_lds_dwordx4 v[246:247], off
	s_branch .Lr687_skip

.LBB0_700:
	s_lshl_b32 s8, s36, 19
	s_cmp_gt_i32 s82, s86
	s_cbranch_scc1 .LBB0_781
	s_sub_i32 s36, s2, s43
	s_sub_i32 s84, 0, s42
	s_cmp_ge_i32 s82, s42
	s_mov_b64 s[0:1], -1
	s_cbranch_scc0 .LBB0_704
	s_branch .LBB0_703
	s_nop 0
	s_nop 0
	s_nop 0
	s_nop 0
	s_nop 0
	s_nop 0
	s_nop 0
	s_nop 0
	s_nop 0
	s_nop 0
	s_nop 0
	s_nop 0
	s_nop 0
	s_nop 0
	s_nop 0
	s_nop 0
	s_nop 0
	s_nop 0
	s_nop 0
	s_nop 0
	s_nop 0
	s_nop 0
	s_nop 0
	s_nop 0
	s_nop 0
	s_nop 0
	s_nop 0
	s_nop 0
	s_nop 0
	s_nop 0
	s_nop 0
	s_nop 0
	s_nop 0
	s_nop 0
	s_nop 0

.Lx791_pd:
	s_lshl_b32 s0, s81, 14
	s_add_i32 s0, s0, 0
	v_add_u32_e32 v0, s0, v140
	s_mov_b32 m0, s100
	s_cmp_eq_u32 s32, 0
	s_waitcnt vmcnt(0)
	s_barrier
	ds_read_b128 v[70:73], v0
	ds_read_b128 v[74:77], v0 offset:4096
	ds_read_b128 v[78:81], v197
	ds_read_b128 v[82:85], v197 offset:4096
	ds_read_b128 v[86:89], v0 offset:8192
	ds_read_b128 v[94:97], v0 offset:12288
	s_cbranch_scc1 .Lx791_body
	global_load_lds_dwordx4 v[240:241], off
	s_add_i32 m0, s100, 0x400
	s_nop 0
	global_load_lds_dwordx4 v[242:243], off
	s_mov_b32 m0, s101
	s_nop 0
	global_load_lds_dwordx4 v[244:245], off
	s_add_i32 m0, s101, 0x400
	s_nop 0
	global_load_lds_dwordx4 v[246:247], off
	s_branch .Lx791_body
